# baseline (speedup 1.0000x reference)
.LBB0_10:
	s_or_b64 exec, exec, s[2:3]
	v_cmp_gt_u32_e32 vcc, 48, v0
	s_mov_b64 s[10:11], 0
	s_mov_b64 s[8:9], 0
	s_waitcnt lgkmcnt(0)
	s_barrier
	s_and_saveexec_b64 s[12:13], vcc
	s_cbranch_execz .LBB0_14
	v_and_b32_e32 v7, 3, v0
	v_lshrrev_b32_e32 v6, 2, v0
	v_lshlrev_b32_e32 v1, 4, v7
	v_lshl_or_b32 v2, v6, 6, v1
	ds_read_b128 v[2:5], v2 offset:24576
	v_cmp_eq_u32_e32 vcc, 3, v7
	s_waitcnt lgkmcnt(0)
	v_cvt_f32_f16_sdwa v8, v2 dst_sel:DWORD dst_unused:UNUSED_PAD src0_sel:WORD_1
	v_cvt_f32_f16_sdwa v9, v3 dst_sel:DWORD dst_unused:UNUSED_PAD src0_sel:WORD_1
	v_cvt_f32_f16_e32 v10, v4
	v_cvt_f32_f16_sdwa v11, v4 dst_sel:DWORD dst_unused:UNUSED_PAD src0_sel:WORD_1
	v_mul_f32_e32 v8, v8, v8
	v_fma_mix_f32 v8, v2, v2, v8 op_sel_hi:[1,1,0]
	v_cndmask_b32_e64 v7, v9, 0, vcc
	v_fma_mix_f32 v8, v3, v3, v8 op_sel_hi:[1,1,0]
	v_cndmask_b32_e64 v9, v10, 0, vcc
	v_fmac_f32_e32 v8, v7, v7
	v_cvt_f32_f16_e32 v7, v5
	v_cvt_f32_f16_sdwa v10, v5 dst_sel:DWORD dst_unused:UNUSED_PAD src0_sel:WORD_1
	v_fmac_f32_e32 v8, v9, v9
	v_cndmask_b32_e64 v9, v11, 0, vcc
	v_fmac_f32_e32 v8, v9, v9
	v_cndmask_b32_e64 v7, v7, 0, vcc
	v_fmac_f32_e32 v8, v7, v7
	v_cndmask_b32_e64 v7, v10, 0, vcc
	v_fmac_f32_e32 v8, v7, v7
	s_nop 1
	v_add_f32_dpp v7, v8, v8 quad_perm:[1,0,3,2] row_mask:0xf bank_mask:0xf
	s_nop 1
	v_add_f32_dpp v8, v7, v7 quad_perm:[2,3,0,1] row_mask:0xf bank_mask:0xf
	s_and_saveexec_b64 s[2:3], vcc
	s_cbranch_execz .LBB0_13
	s_waitcnt lgkmcnt(0)
	v_mov_b32_e32 v4, v8
	s_mov_b32 s8, 0.5
	v_fma_mixlo_f16 v5, v4, s8, 0
	v_fma_mixlo_f16 v5, v4, s8, -v5 op_sel_hi:[0,0,1]
	v_fma_mixhi_f16 v3, v4, s8, 0
	s_movk_i32 s8, 0x4c00
	v_pack_b32_f16 v4, v5, s8
	v_mov_b32_e32 v5, 0

.LBB0_21:
	s_or_b64 exec, exec, s[2:3]
	s_movk_i32 s2, 0x60
	v_cmp_gt_u32_e32 vcc, s2, v0
	s_waitcnt lgkmcnt(0)
	s_barrier
	s_and_saveexec_b64 s[10:11], vcc
	s_cbranch_execz .LBB0_25
	v_and_b32_e32 v7, 3, v0
	v_lshrrev_b32_e32 v6, 2, v0
	v_lshlrev_b32_e32 v1, 4, v7
	v_lshl_or_b32 v2, v6, 6, v1
	ds_read_b128 v[2:5], v2 offset:24576
	v_cmp_eq_u32_e32 vcc, 3, v7
	s_waitcnt lgkmcnt(0)
	v_cvt_f32_f16_sdwa v8, v2 dst_sel:DWORD dst_unused:UNUSED_PAD src0_sel:WORD_1
	v_cvt_f32_f16_sdwa v9, v3 dst_sel:DWORD dst_unused:UNUSED_PAD src0_sel:WORD_1
	v_cvt_f32_f16_e32 v10, v4
	v_cvt_f32_f16_sdwa v11, v4 dst_sel:DWORD dst_unused:UNUSED_PAD src0_sel:WORD_1
	v_mul_f32_e32 v8, v8, v8
	v_fma_mix_f32 v8, v2, v2, v8 op_sel_hi:[1,1,0]
	v_cndmask_b32_e64 v7, v9, 0, vcc
	v_fma_mix_f32 v8, v3, v3, v8 op_sel_hi:[1,1,0]
	v_cndmask_b32_e64 v9, v10, 0, vcc
	v_fmac_f32_e32 v8, v7, v7
	v_cvt_f32_f16_e32 v7, v5
	v_cvt_f32_f16_sdwa v10, v5 dst_sel:DWORD dst_unused:UNUSED_PAD src0_sel:WORD_1
	v_fmac_f32_e32 v8, v9, v9
	v_cndmask_b32_e64 v9, v11, 0, vcc
	v_fmac_f32_e32 v8, v9, v9
	v_cndmask_b32_e64 v7, v7, 0, vcc
	v_fmac_f32_e32 v8, v7, v7
	v_cndmask_b32_e64 v7, v10, 0, vcc
	v_fmac_f32_e32 v8, v7, v7
	s_nop 1
	v_add_f32_dpp v7, v8, v8 quad_perm:[1,0,3,2] row_mask:0xf bank_mask:0xf
	s_nop 1
	v_add_f32_dpp v8, v7, v7 quad_perm:[2,3,0,1] row_mask:0xf bank_mask:0xf
	s_and_saveexec_b64 s[2:3], vcc
	s_cbranch_execz .LBB0_24
	s_waitcnt lgkmcnt(0)
	v_mov_b32_e32 v4, v8
	s_mov_b32 s13, 0.5
	v_fma_mixlo_f16 v5, v4, s13, 0
	v_fma_mixlo_f16 v5, v4, s13, -v5 op_sel_hi:[0,0,1]
	v_fma_mixhi_f16 v3, v4, s13, 0
	s_movk_i32 s13, 0x4c00
	v_pack_b32_f16 v4, v5, s13
	v_mov_b32_e32 v5, 0

.LBB1_32:
	s_or_b64 exec, exec, s[8:9]
	s_waitcnt vmcnt(0)
	v_readfirstlane_b32 s1, v5
	v_readfirstlane_b32 s0, v4
	s_mov_b32 s7, 0xf000000
	s_nop 0
	v_lshl_add_u64 v[4:5], s[0:1], 0, v[2:3]
	v_and_b32_e32 v3, 0xff000000, v5
	v_mov_b32_e32 v2, 0
	v_cmp_eq_u64_e32 vcc, s[6:7], v[2:3]
	s_and_b64 exec, exec, vcc
	s_cbranch_execz .LBB1_34
	v_lshl_add_u64 v[0:1], v[4:5], 0, v[0:1]
	v_and_b32_e32 v1, 0xffffff, v1
	v_cvt_f64_u32_e32 v[4:5], v1
	v_ldexp_f64 v[4:5], v[4:5], 32
	v_cvt_f64_u32_e32 v[0:1], v0
	v_add_f64 v[0:1], v[4:5], v[0:1]
	s_movk_i32 s0, 0xffec
	v_ldexp_f64 v[0:1], v[0:1], s0
	s_mov_b32 s0, 0xa88f4696
	s_mov_b32 s1, 0x3eb0db20
	v_mul_f64 v[0:1], v[0:1], s[0:1]
	v_cvt_f32_f64_e32 v0, v[0:1]
	global_store_dword v2, v0, s[2:3]
